# t18
# speedup vs baseline: 1.0644x; 1.0644x over previous
_Z11align_fusedPKfS0_PKiPf:
	s_load_dwordx8 s[4:11], s[0:1], 0x0
	s_sub_u32 s2, 0x1fff, s2
	s_mul_i32 s12, s2, 0x5dc0
	v_and_b32_e32 v7, 63, v0
	v_readfirstlane_b32 s13, v0
	v_lshlrev_b32_e32 v1, 4, v7
	v_mul_u32_u24_e32 v3, 12, v7
	s_mul_i32 s18, s13, 96
	s_mul_i32 s3, s13, 6
	s_sub_u32 s3, 0x49c, s3
	v_cmp_gt_u32_e64 s[14:15], s3, v7
	v_add_u32_e32 v2, s18, v1
	v_add_u32_e32 v3, s18, v3
	v_add_u32_e32 v4, 0x600, v3
	s_add_u32 s12, s12, s18
	s_add_u32 s12, s12, 0x800
	s_waitcnt lgkmcnt(0)
	s_add_u32 s4, s4, s12
	s_addc_u32 s5, s5, 0
	s_add_u32 s10, s10, s12
	s_addc_u32 s11, s11, 0
	s_cmp_lg_u32 s13, 0
	s_cbranch_scc1 .Lbulk_waves
	v_lshlrev_b32_e32 v5, 2, v7
	global_load_dword v5, v5, s[8:9]
	global_load_dwordx3 v[44:46], v3, s[6:7] nt
	global_load_dwordx4 v[8:11], v1, s[4:5] offset:-2048 nt
	global_load_dwordx4 v[12:15], v1, s[4:5] offset:-1024 nt
	global_load_dwordx4 v[16:19], v1, s[4:5] offset:0 nt
	global_load_dwordx4 v[20:23], v1, s[4:5] offset:1024 nt
	global_load_dwordx4 v[24:27], v1, s[4:5] offset:2048 nt
	global_load_dwordx4 v[28:31], v1, s[4:5] offset:3072 nt
	s_mov_b32 s20, 0
	s_mov_b32 s21, 0x10000
	s_mov_b32 s22, 0
	s_mov_b32 s23, 0x20000
	s_mov_b32 s24, 0
	s_mov_b32 s25, 0x40000
	s_mov_b32 s26, 0
	s_mov_b32 s27, 0x80000
	s_waitcnt vmcnt(6)
	v_mul_u32_u24_e32 v5, 12, v5
	v_add_f32_dpp v52, v44, v44 quad_perm:[1,0,3,2] row_mask:0xf bank_mask:0xf
	v_add_f32_dpp v53, v45, v45 quad_perm:[1,0,3,2] row_mask:0xf bank_mask:0xf
	v_add_f32_dpp v54, v46, v46 quad_perm:[1,0,3,2] row_mask:0xf bank_mask:0xf
	v_add_f32_dpp v52, v52, v52 quad_perm:[2,3,0,1] row_mask:0xf bank_mask:0xf
	v_add_f32_dpp v53, v53, v53 quad_perm:[2,3,0,1] row_mask:0xf bank_mask:0xf
	v_add_f32_dpp v54, v54, v54 quad_perm:[2,3,0,1] row_mask:0xf bank_mask:0xf
	v_add_f32_dpp v52, v52, v52 row_half_mirror row_mask:0xf bank_mask:0xf
	v_add_f32_dpp v53, v53, v53 row_half_mirror row_mask:0xf bank_mask:0xf
	v_add_f32_dpp v54, v54, v54 row_half_mirror row_mask:0xf bank_mask:0xf
	v_add_f32_dpp v52, v52, v52 row_mirror row_mask:0xf bank_mask:0xf
	v_add_f32_dpp v53, v53, v53 row_mirror row_mask:0xf bank_mask:0xf
	v_add_f32_dpp v54, v54, v54 row_mirror row_mask:0xf bank_mask:0xf
	v_add_f32_dpp v52, v52, v52 row_bcast:15 row_mask:0xa bank_mask:0xf
	v_add_f32_dpp v53, v53, v53 row_bcast:15 row_mask:0xa bank_mask:0xf
	v_add_f32_dpp v54, v54, v54 row_bcast:15 row_mask:0xa bank_mask:0xf
	v_add_f32_dpp v52, v52, v52 row_bcast:31 row_mask:0xc bank_mask:0xf
	v_add_f32_dpp v53, v53, v53 row_bcast:31 row_mask:0xc bank_mask:0xf
	v_add_f32_dpp v54, v54, v54 row_bcast:31 row_mask:0xc bank_mask:0xf
	v_readlane_b32 s28, v52, 63
	v_readlane_b32 s29, v53, 63
	v_readlane_b32 s30, v54, 63
	v_mov_b32_e32 v52, s28
	v_mov_b32_e32 v53, s29
	v_mov_b32_e32 v54, s30
	v_fmac_f32_e32 v44, 0xbc800000, v52
	v_fmac_f32_e32 v45, 0xbc800000, v53
	v_fmac_f32_e32 v46, 0xbc800000, v54
	s_waitcnt vmcnt(0)
	ds_write_b128 v2, v[8:11]
	ds_write_b128 v2, v[12:15] offset:1024
	ds_write_b128 v2, v[16:19] offset:2048
	ds_write_b128 v2, v[20:23] offset:3072
	ds_write_b128 v2, v[24:27] offset:4096
	ds_write_b128 v2, v[28:31] offset:5120
	s_waitcnt lgkmcnt(0)
	s_barrier
	s_setprio 3
	ds_read_b32 v48, v5
	ds_read_b32 v49, v5 offset:4
	ds_read_b32 v50, v5 offset:8
	s_waitcnt lgkmcnt(0)
	v_add_f32_dpp v52, v48, v48 quad_perm:[1,0,3,2] row_mask:0xf bank_mask:0xf
	v_add_f32_dpp v53, v49, v49 quad_perm:[1,0,3,2] row_mask:0xf bank_mask:0xf
	v_add_f32_dpp v54, v50, v50 quad_perm:[1,0,3,2] row_mask:0xf bank_mask:0xf
	v_add_f32_dpp v52, v52, v52 quad_perm:[2,3,0,1] row_mask:0xf bank_mask:0xf
	v_add_f32_dpp v53, v53, v53 quad_perm:[2,3,0,1] row_mask:0xf bank_mask:0xf
	v_add_f32_dpp v54, v54, v54 quad_perm:[2,3,0,1] row_mask:0xf bank_mask:0xf
	v_add_f32_dpp v52, v52, v52 row_half_mirror row_mask:0xf bank_mask:0xf
	v_add_f32_dpp v53, v53, v53 row_half_mirror row_mask:0xf bank_mask:0xf
	v_add_f32_dpp v54, v54, v54 row_half_mirror row_mask:0xf bank_mask:0xf
	v_add_f32_dpp v52, v52, v52 row_mirror row_mask:0xf bank_mask:0xf
	v_add_f32_dpp v53, v53, v53 row_mirror row_mask:0xf bank_mask:0xf
	v_add_f32_dpp v54, v54, v54 row_mirror row_mask:0xf bank_mask:0xf
	v_add_f32_dpp v52, v52, v52 row_bcast:15 row_mask:0xa bank_mask:0xf
	v_add_f32_dpp v53, v53, v53 row_bcast:15 row_mask:0xa bank_mask:0xf
	v_add_f32_dpp v54, v54, v54 row_bcast:15 row_mask:0xa bank_mask:0xf
	v_add_f32_dpp v52, v52, v52 row_bcast:31 row_mask:0xc bank_mask:0xf
	v_add_f32_dpp v53, v53, v53 row_bcast:31 row_mask:0xc bank_mask:0xf
	v_add_f32_dpp v54, v54, v54 row_bcast:31 row_mask:0xc bank_mask:0xf
	v_readlane_b32 s32, v52, 63
	v_readlane_b32 s33, v53, 63
	v_readlane_b32 s34, v54, 63
	v_mov_b32_e32 v52, s32
	v_mov_b32_e32 v53, s33
	v_mov_b32_e32 v54, s34
	v_fmac_f32_e32 v48, 0xbc800000, v52
	v_fmac_f32_e32 v49, 0xbc800000, v53
	v_fmac_f32_e32 v50, 0xbc800000, v54
	v_mul_f32_e32 v52, v48, v44
	v_mul_f32_e32 v53, v48, v45
	v_mul_f32_e32 v54, v48, v46
	v_mul_f32_e32 v55, v49, v44
	v_mul_f32_e32 v56, v49, v45
	v_mul_f32_e32 v57, v49, v46
	v_mul_f32_e32 v58, v50, v44
	v_mul_f32_e32 v59, v50, v45
	v_mul_f32_e32 v60, v50, v46
	v_add_f32_dpp v52, v52, v52 quad_perm:[1,0,3,2] row_mask:0xf bank_mask:0xf
	v_add_f32_dpp v53, v53, v53 quad_perm:[1,0,3,2] row_mask:0xf bank_mask:0xf
	v_add_f32_dpp v54, v54, v54 quad_perm:[1,0,3,2] row_mask:0xf bank_mask:0xf
	v_add_f32_dpp v55, v55, v55 quad_perm:[1,0,3,2] row_mask:0xf bank_mask:0xf
	v_add_f32_dpp v56, v56, v56 quad_perm:[1,0,3,2] row_mask:0xf bank_mask:0xf
	v_add_f32_dpp v57, v57, v57 quad_perm:[1,0,3,2] row_mask:0xf bank_mask:0xf
	v_add_f32_dpp v58, v58, v58 quad_perm:[1,0,3,2] row_mask:0xf bank_mask:0xf
	v_add_f32_dpp v59, v59, v59 quad_perm:[1,0,3,2] row_mask:0xf bank_mask:0xf
	v_add_f32_dpp v60, v60, v60 quad_perm:[1,0,3,2] row_mask:0xf bank_mask:0xf
	v_add_f32_dpp v52, v52, v52 quad_perm:[2,3,0,1] row_mask:0xf bank_mask:0xf
	v_add_f32_dpp v53, v53, v53 quad_perm:[2,3,0,1] row_mask:0xf bank_mask:0xf
	v_add_f32_dpp v54, v54, v54 quad_perm:[2,3,0,1] row_mask:0xf bank_mask:0xf
	v_add_f32_dpp v55, v55, v55 quad_perm:[2,3,0,1] row_mask:0xf bank_mask:0xf
	v_add_f32_dpp v56, v56, v56 quad_perm:[2,3,0,1] row_mask:0xf bank_mask:0xf
	v_add_f32_dpp v57, v57, v57 quad_perm:[2,3,0,1] row_mask:0xf bank_mask:0xf
	v_add_f32_dpp v58, v58, v58 quad_perm:[2,3,0,1] row_mask:0xf bank_mask:0xf
	v_add_f32_dpp v59, v59, v59 quad_perm:[2,3,0,1] row_mask:0xf bank_mask:0xf
	v_add_f32_dpp v60, v60, v60 quad_perm:[2,3,0,1] row_mask:0xf bank_mask:0xf
	v_add_f32_dpp v52, v52, v52 row_half_mirror row_mask:0xf bank_mask:0xf
	v_add_f32_dpp v53, v53, v53 row_half_mirror row_mask:0xf bank_mask:0xf
	v_add_f32_dpp v54, v54, v54 row_half_mirror row_mask:0xf bank_mask:0xf
	v_add_f32_dpp v55, v55, v55 row_half_mirror row_mask:0xf bank_mask:0xf
	v_add_f32_dpp v56, v56, v56 row_half_mirror row_mask:0xf bank_mask:0xf
	v_add_f32_dpp v57, v57, v57 row_half_mirror row_mask:0xf bank_mask:0xf
	v_add_f32_dpp v58, v58, v58 row_half_mirror row_mask:0xf bank_mask:0xf
	v_add_f32_dpp v59, v59, v59 row_half_mirror row_mask:0xf bank_mask:0xf
	v_add_f32_dpp v60, v60, v60 row_half_mirror row_mask:0xf bank_mask:0xf
	v_add_f32_dpp v52, v52, v52 row_mirror row_mask:0xf bank_mask:0xf
	v_add_f32_dpp v53, v53, v53 row_mirror row_mask:0xf bank_mask:0xf
	v_add_f32_dpp v54, v54, v54 row_mirror row_mask:0xf bank_mask:0xf
	v_add_f32_dpp v55, v55, v55 row_mirror row_mask:0xf bank_mask:0xf
	v_add_f32_dpp v56, v56, v56 row_mirror row_mask:0xf bank_mask:0xf
	v_add_f32_dpp v57, v57, v57 row_mirror row_mask:0xf bank_mask:0xf
	v_add_f32_dpp v58, v58, v58 row_mirror row_mask:0xf bank_mask:0xf
	v_add_f32_dpp v59, v59, v59 row_mirror row_mask:0xf bank_mask:0xf
	v_add_f32_dpp v60, v60, v60 row_mirror row_mask:0xf bank_mask:0xf
	v_add_f32_dpp v52, v52, v52 row_bcast:15 row_mask:0xa bank_mask:0xf
	v_add_f32_dpp v53, v53, v53 row_bcast:15 row_mask:0xa bank_mask:0xf
	v_add_f32_dpp v54, v54, v54 row_bcast:15 row_mask:0xa bank_mask:0xf
	v_add_f32_dpp v55, v55, v55 row_bcast:15 row_mask:0xa bank_mask:0xf
	v_add_f32_dpp v56, v56, v56 row_bcast:15 row_mask:0xa bank_mask:0xf
	v_add_f32_dpp v57, v57, v57 row_bcast:15 row_mask:0xa bank_mask:0xf
	v_add_f32_dpp v58, v58, v58 row_bcast:15 row_mask:0xa bank_mask:0xf
	v_add_f32_dpp v59, v59, v59 row_bcast:15 row_mask:0xa bank_mask:0xf
	v_add_f32_dpp v60, v60, v60 row_bcast:15 row_mask:0xa bank_mask:0xf
	v_add_f32_dpp v52, v52, v52 row_bcast:31 row_mask:0xc bank_mask:0xf
	v_add_f32_dpp v53, v53, v53 row_bcast:31 row_mask:0xc bank_mask:0xf
	v_add_f32_dpp v54, v54, v54 row_bcast:31 row_mask:0xc bank_mask:0xf
	v_add_f32_dpp v55, v55, v55 row_bcast:31 row_mask:0xc bank_mask:0xf
	v_add_f32_dpp v56, v56, v56 row_bcast:31 row_mask:0xc bank_mask:0xf
	v_add_f32_dpp v57, v57, v57 row_bcast:31 row_mask:0xc bank_mask:0xf
	v_add_f32_dpp v58, v58, v58 row_bcast:31 row_mask:0xc bank_mask:0xf
	v_add_f32_dpp v59, v59, v59 row_bcast:31 row_mask:0xc bank_mask:0xf
	v_add_f32_dpp v60, v60, v60 row_bcast:31 row_mask:0xc bank_mask:0xf
	v_cndmask_b32_e64 v52, v52, v55, s[22:23]
	v_cndmask_b32_e64 v53, v53, v56, s[22:23]
	v_cndmask_b32_e64 v54, v54, v57, s[22:23]
	v_cndmask_b32_e64 v52, v52, v58, s[24:25]
	v_cndmask_b32_e64 v53, v53, v59, s[24:25]
	v_cndmask_b32_e64 v54, v54, v60, s[24:25]
	v_cndmask_b32_e64 v52, v52, 0, s[26:27]
	v_cndmask_b32_e64 v53, v53, 0, s[26:27]
	v_cndmask_b32_e64 v54, v54, 0, s[26:27]
	v_cndmask_b32_e64 v40, 0, 1.0, s[20:21]
	v_cndmask_b32_e64 v41, 0, 1.0, s[22:23]
	v_cndmask_b32_e64 v42, 0, 1.0, s[24:25]
	v_mul_f32_e32 v55, v52, v52
	v_mul_f32_e32 v56, v53, v53
	v_mul_f32_e32 v57, v52, v53
	v_add_f32_dpp v55, v55, v55 quad_perm:[1,0,3,2] row_mask:0xf bank_mask:0xf
	v_add_f32_dpp v56, v56, v56 quad_perm:[1,0,3,2] row_mask:0xf bank_mask:0xf
	v_add_f32_dpp v57, v57, v57 quad_perm:[1,0,3,2] row_mask:0xf bank_mask:0xf
	v_add_f32_dpp v55, v55, v55 quad_perm:[2,3,0,1] row_mask:0xf bank_mask:0xf
	v_add_f32_dpp v56, v56, v56 quad_perm:[2,3,0,1] row_mask:0xf bank_mask:0xf
	v_add_f32_dpp v57, v57, v57 quad_perm:[2,3,0,1] row_mask:0xf bank_mask:0xf
	v_sub_f32_e32 v60, v56, v55
	v_mul_f32_e32 v58, v57, v57
	v_cmp_gt_f32_e32 vcc, 0, v60
	v_mul_f32_e32 v59, v60, v60
	v_fmac_f32_e32 v59, 4.0, v58
	v_sqrt_f32_e32 v59, v59
	s_nop 0
	v_add_f32_e64 v59, |v60|, v59
	v_add_f32_e32 v59, 0x0da24260, v59
	v_rcp_f32_e32 v59, v59
	v_add_f32_e32 v58, v57, v57
	v_mul_f32_e32 v59, v58, v59
	v_cndmask_b32_e64 v59, v59, -v59, vcc
	v_fma_f32 v58, v59, v59, 1.0
	v_rsq_f32_e32 v61, v58
	s_nop 0
	v_mul_f32_e32 v62, v61, v59
	v_mul_f32_e32 v55, v62, v53
	v_mul_f32_e32 v56, v62, v52
	v_fma_f32 v52, v61, v52, -v55
	v_fma_f32 v53, v61, v53, v56
	v_mul_f32_e32 v55, v52, v52
	v_mul_f32_e32 v56, v54, v54
	v_mul_f32_e32 v57, v52, v54
	v_add_f32_dpp v55, v55, v55 quad_perm:[1,0,3,2] row_mask:0xf bank_mask:0xf
	v_add_f32_dpp v56, v56, v56 quad_perm:[1,0,3,2] row_mask:0xf bank_mask:0xf
	v_add_f32_dpp v57, v57, v57 quad_perm:[1,0,3,2] row_mask:0xf bank_mask:0xf
	v_add_f32_dpp v55, v55, v55 quad_perm:[2,3,0,1] row_mask:0xf bank_mask:0xf
	v_add_f32_dpp v56, v56, v56 quad_perm:[2,3,0,1] row_mask:0xf bank_mask:0xf
	v_add_f32_dpp v57, v57, v57 quad_perm:[2,3,0,1] row_mask:0xf bank_mask:0xf
	v_sub_f32_e32 v60, v56, v55
	v_mul_f32_e32 v58, v57, v57
	v_cmp_gt_f32_e32 vcc, 0, v60
	v_mul_f32_e32 v59, v60, v60
	v_fmac_f32_e32 v59, 4.0, v58
	v_sqrt_f32_e32 v59, v59
	v_mul_f32_e32 v63, v62, v41
	v_mul_f32_e32 v43, v62, v40
	v_fma_f32 v40, v61, v40, -v63
	v_fma_f32 v41, v61, v41, v43
	v_add_f32_e64 v59, |v60|, v59
	v_add_f32_e32 v59, 0x0da24260, v59
	v_rcp_f32_e32 v59, v59
	v_add_f32_e32 v58, v57, v57
	v_mul_f32_e32 v59, v58, v59
	v_cndmask_b32_e64 v59, v59, -v59, vcc
	v_fma_f32 v58, v59, v59, 1.0
	v_rsq_f32_e32 v61, v58
	s_nop 0
	v_mul_f32_e32 v62, v61, v59
	v_mul_f32_e32 v55, v62, v54
	v_mul_f32_e32 v56, v62, v52
	v_fma_f32 v52, v61, v52, -v55
	v_fma_f32 v54, v61, v54, v56
	v_mul_f32_e32 v55, v53, v53
	v_mul_f32_e32 v56, v54, v54
	v_mul_f32_e32 v57, v53, v54
	v_add_f32_dpp v55, v55, v55 quad_perm:[1,0,3,2] row_mask:0xf bank_mask:0xf
	v_add_f32_dpp v56, v56, v56 quad_perm:[1,0,3,2] row_mask:0xf bank_mask:0xf
	v_add_f32_dpp v57, v57, v57 quad_perm:[1,0,3,2] row_mask:0xf bank_mask:0xf
	v_add_f32_dpp v55, v55, v55 quad_perm:[2,3,0,1] row_mask:0xf bank_mask:0xf
	v_add_f32_dpp v56, v56, v56 quad_perm:[2,3,0,1] row_mask:0xf bank_mask:0xf
	v_add_f32_dpp v57, v57, v57 quad_perm:[2,3,0,1] row_mask:0xf bank_mask:0xf
	v_sub_f32_e32 v60, v56, v55
	v_mul_f32_e32 v58, v57, v57
	v_cmp_gt_f32_e32 vcc, 0, v60
	v_mul_f32_e32 v59, v60, v60
	v_fmac_f32_e32 v59, 4.0, v58
	v_sqrt_f32_e32 v59, v59
	v_mul_f32_e32 v63, v62, v42
	v_mul_f32_e32 v43, v62, v40
	v_fma_f32 v40, v61, v40, -v63
	v_fma_f32 v42, v61, v42, v43
	v_add_f32_e64 v59, |v60|, v59
	v_add_f32_e32 v59, 0x0da24260, v59
	v_rcp_f32_e32 v59, v59
	v_add_f32_e32 v58, v57, v57
	v_mul_f32_e32 v59, v58, v59
	v_cndmask_b32_e64 v59, v59, -v59, vcc
	v_fma_f32 v58, v59, v59, 1.0
	v_rsq_f32_e32 v61, v58
	s_nop 0
	v_mul_f32_e32 v62, v61, v59
	v_mul_f32_e32 v55, v62, v54
	v_mul_f32_e32 v56, v62, v53
	v_fma_f32 v53, v61, v53, -v55
	v_fma_f32 v54, v61, v54, v56
	v_mul_f32_e32 v55, v52, v52
	v_mul_f32_e32 v56, v53, v53
	v_mul_f32_e32 v57, v52, v53
	v_add_f32_dpp v55, v55, v55 quad_perm:[1,0,3,2] row_mask:0xf bank_mask:0xf
	v_add_f32_dpp v56, v56, v56 quad_perm:[1,0,3,2] row_mask:0xf bank_mask:0xf
	v_add_f32_dpp v57, v57, v57 quad_perm:[1,0,3,2] row_mask:0xf bank_mask:0xf
	v_add_f32_dpp v55, v55, v55 quad_perm:[2,3,0,1] row_mask:0xf bank_mask:0xf
	v_add_f32_dpp v56, v56, v56 quad_perm:[2,3,0,1] row_mask:0xf bank_mask:0xf
	v_add_f32_dpp v57, v57, v57 quad_perm:[2,3,0,1] row_mask:0xf bank_mask:0xf
	v_sub_f32_e32 v60, v56, v55
	v_mul_f32_e32 v58, v57, v57
	v_cmp_gt_f32_e32 vcc, 0, v60
	v_mul_f32_e32 v59, v60, v60
	v_fmac_f32_e32 v59, 4.0, v58
	v_sqrt_f32_e32 v59, v59
	v_mul_f32_e32 v63, v62, v42
	v_mul_f32_e32 v43, v62, v41
	v_fma_f32 v41, v61, v41, -v63
	v_fma_f32 v42, v61, v42, v43
	v_add_f32_e64 v59, |v60|, v59
	v_add_f32_e32 v59, 0x0da24260, v59
	v_rcp_f32_e32 v59, v59
	v_add_f32_e32 v58, v57, v57
	v_mul_f32_e32 v59, v58, v59
	v_cndmask_b32_e64 v59, v59, -v59, vcc
	v_fma_f32 v58, v59, v59, 1.0
	v_rsq_f32_e32 v61, v58
	s_nop 0
	v_mul_f32_e32 v62, v61, v59
	v_mul_f32_e32 v55, v62, v53
	v_mul_f32_e32 v56, v62, v52
	v_fma_f32 v52, v61, v52, -v55
	v_fma_f32 v53, v61, v53, v56
	v_mul_f32_e32 v55, v52, v52
	v_mul_f32_e32 v56, v54, v54
	v_mul_f32_e32 v57, v52, v54
	v_add_f32_dpp v55, v55, v55 quad_perm:[1,0,3,2] row_mask:0xf bank_mask:0xf
	v_add_f32_dpp v56, v56, v56 quad_perm:[1,0,3,2] row_mask:0xf bank_mask:0xf
	v_add_f32_dpp v57, v57, v57 quad_perm:[1,0,3,2] row_mask:0xf bank_mask:0xf
	v_add_f32_dpp v55, v55, v55 quad_perm:[2,3,0,1] row_mask:0xf bank_mask:0xf
	v_add_f32_dpp v56, v56, v56 quad_perm:[2,3,0,1] row_mask:0xf bank_mask:0xf
	v_add_f32_dpp v57, v57, v57 quad_perm:[2,3,0,1] row_mask:0xf bank_mask:0xf
	v_sub_f32_e32 v60, v56, v55
	v_mul_f32_e32 v58, v57, v57
	v_cmp_gt_f32_e32 vcc, 0, v60
	v_mul_f32_e32 v59, v60, v60
	v_fmac_f32_e32 v59, 4.0, v58
	v_sqrt_f32_e32 v59, v59
	v_mul_f32_e32 v63, v62, v41
	v_mul_f32_e32 v43, v62, v40
	v_fma_f32 v40, v61, v40, -v63
	v_fma_f32 v41, v61, v41, v43
	v_add_f32_e64 v59, |v60|, v59
	v_add_f32_e32 v59, 0x0da24260, v59
	v_rcp_f32_e32 v59, v59
	v_add_f32_e32 v58, v57, v57
	v_mul_f32_e32 v59, v58, v59
	v_cndmask_b32_e64 v59, v59, -v59, vcc
	v_fma_f32 v58, v59, v59, 1.0
	v_rsq_f32_e32 v61, v58
	s_nop 0
	v_mul_f32_e32 v62, v61, v59
	v_mul_f32_e32 v55, v62, v54
	v_mul_f32_e32 v56, v62, v52
	v_fma_f32 v52, v61, v52, -v55
	v_fma_f32 v54, v61, v54, v56
	v_mul_f32_e32 v55, v53, v53
	v_mul_f32_e32 v56, v54, v54
	v_mul_f32_e32 v57, v53, v54
	v_add_f32_dpp v55, v55, v55 quad_perm:[1,0,3,2] row_mask:0xf bank_mask:0xf
	v_add_f32_dpp v56, v56, v56 quad_perm:[1,0,3,2] row_mask:0xf bank_mask:0xf
	v_add_f32_dpp v57, v57, v57 quad_perm:[1,0,3,2] row_mask:0xf bank_mask:0xf
	v_add_f32_dpp v55, v55, v55 quad_perm:[2,3,0,1] row_mask:0xf bank_mask:0xf
	v_add_f32_dpp v56, v56, v56 quad_perm:[2,3,0,1] row_mask:0xf bank_mask:0xf
	v_add_f32_dpp v57, v57, v57 quad_perm:[2,3,0,1] row_mask:0xf bank_mask:0xf
	v_sub_f32_e32 v60, v56, v55
	v_mul_f32_e32 v58, v57, v57
	v_cmp_gt_f32_e32 vcc, 0, v60
	v_mul_f32_e32 v59, v60, v60
	v_fmac_f32_e32 v59, 4.0, v58
	v_sqrt_f32_e32 v59, v59
	v_mul_f32_e32 v63, v62, v42
	v_mul_f32_e32 v43, v62, v40
	v_fma_f32 v40, v61, v40, -v63
	v_fma_f32 v42, v61, v42, v43
	v_add_f32_e64 v59, |v60|, v59
	v_add_f32_e32 v59, 0x0da24260, v59
	v_rcp_f32_e32 v59, v59
	v_add_f32_e32 v58, v57, v57
	v_mul_f32_e32 v59, v58, v59
	v_cndmask_b32_e64 v59, v59, -v59, vcc
	v_fma_f32 v58, v59, v59, 1.0
	v_rsq_f32_e32 v61, v58
	s_nop 0
	v_mul_f32_e32 v62, v61, v59
	v_mul_f32_e32 v55, v62, v54
	v_mul_f32_e32 v56, v62, v53
	v_fma_f32 v53, v61, v53, -v55
	v_fma_f32 v54, v61, v54, v56
	v_mul_f32_e32 v55, v52, v52
	v_mul_f32_e32 v56, v53, v53
	v_mul_f32_e32 v57, v52, v53
	v_add_f32_dpp v55, v55, v55 quad_perm:[1,0,3,2] row_mask:0xf bank_mask:0xf
	v_add_f32_dpp v56, v56, v56 quad_perm:[1,0,3,2] row_mask:0xf bank_mask:0xf
	v_add_f32_dpp v57, v57, v57 quad_perm:[1,0,3,2] row_mask:0xf bank_mask:0xf
	v_add_f32_dpp v55, v55, v55 quad_perm:[2,3,0,1] row_mask:0xf bank_mask:0xf
	v_add_f32_dpp v56, v56, v56 quad_perm:[2,3,0,1] row_mask:0xf bank_mask:0xf
	v_add_f32_dpp v57, v57, v57 quad_perm:[2,3,0,1] row_mask:0xf bank_mask:0xf
	v_sub_f32_e32 v60, v56, v55
	v_mul_f32_e32 v58, v57, v57
	v_cmp_gt_f32_e32 vcc, 0, v60
	v_mul_f32_e32 v59, v60, v60
	v_fmac_f32_e32 v59, 4.0, v58
	v_sqrt_f32_e32 v59, v59
	v_mul_f32_e32 v63, v62, v42
	v_mul_f32_e32 v43, v62, v41
	v_fma_f32 v41, v61, v41, -v63
	v_fma_f32 v42, v61, v42, v43
	v_add_f32_e64 v59, |v60|, v59
	v_add_f32_e32 v59, 0x0da24260, v59
	v_rcp_f32_e32 v59, v59
	v_add_f32_e32 v58, v57, v57
	v_mul_f32_e32 v59, v58, v59
	v_cndmask_b32_e64 v59, v59, -v59, vcc
	v_fma_f32 v58, v59, v59, 1.0
	v_rsq_f32_e32 v61, v58
	s_nop 0
	v_mul_f32_e32 v62, v61, v59
	v_mul_f32_e32 v55, v62, v53
	v_mul_f32_e32 v56, v62, v52
	v_fma_f32 v52, v61, v52, -v55
	v_fma_f32 v53, v61, v53, v56
	v_mul_f32_e32 v55, v52, v52
	v_mul_f32_e32 v56, v54, v54
	v_mul_f32_e32 v57, v52, v54
	v_add_f32_dpp v55, v55, v55 quad_perm:[1,0,3,2] row_mask:0xf bank_mask:0xf
	v_add_f32_dpp v56, v56, v56 quad_perm:[1,0,3,2] row_mask:0xf bank_mask:0xf
	v_add_f32_dpp v57, v57, v57 quad_perm:[1,0,3,2] row_mask:0xf bank_mask:0xf
	v_add_f32_dpp v55, v55, v55 quad_perm:[2,3,0,1] row_mask:0xf bank_mask:0xf
	v_add_f32_dpp v56, v56, v56 quad_perm:[2,3,0,1] row_mask:0xf bank_mask:0xf
	v_add_f32_dpp v57, v57, v57 quad_perm:[2,3,0,1] row_mask:0xf bank_mask:0xf
	v_sub_f32_e32 v60, v56, v55
	v_mul_f32_e32 v58, v57, v57
	v_cmp_gt_f32_e32 vcc, 0, v60
	v_mul_f32_e32 v59, v60, v60
	v_fmac_f32_e32 v59, 4.0, v58
	v_sqrt_f32_e32 v59, v59
	v_mul_f32_e32 v63, v62, v41
	v_mul_f32_e32 v43, v62, v40
	v_fma_f32 v40, v61, v40, -v63
	v_fma_f32 v41, v61, v41, v43
	v_add_f32_e64 v59, |v60|, v59
	v_add_f32_e32 v59, 0x0da24260, v59
	v_rcp_f32_e32 v59, v59
	v_add_f32_e32 v58, v57, v57
	v_mul_f32_e32 v59, v58, v59
	v_cndmask_b32_e64 v59, v59, -v59, vcc
	v_fma_f32 v58, v59, v59, 1.0
	v_rsq_f32_e32 v61, v58
	s_nop 0
	v_mul_f32_e32 v62, v61, v59
	v_mul_f32_e32 v55, v62, v54
	v_mul_f32_e32 v56, v62, v52
	v_fma_f32 v52, v61, v52, -v55
	v_fma_f32 v54, v61, v54, v56
	v_mul_f32_e32 v55, v53, v53
	v_mul_f32_e32 v56, v54, v54
	v_mul_f32_e32 v57, v53, v54
	v_add_f32_dpp v55, v55, v55 quad_perm:[1,0,3,2] row_mask:0xf bank_mask:0xf
	v_add_f32_dpp v56, v56, v56 quad_perm:[1,0,3,2] row_mask:0xf bank_mask:0xf
	v_add_f32_dpp v57, v57, v57 quad_perm:[1,0,3,2] row_mask:0xf bank_mask:0xf
	v_add_f32_dpp v55, v55, v55 quad_perm:[2,3,0,1] row_mask:0xf bank_mask:0xf
	v_add_f32_dpp v56, v56, v56 quad_perm:[2,3,0,1] row_mask:0xf bank_mask:0xf
	v_add_f32_dpp v57, v57, v57 quad_perm:[2,3,0,1] row_mask:0xf bank_mask:0xf
	v_sub_f32_e32 v60, v56, v55
	v_mul_f32_e32 v58, v57, v57
	v_cmp_gt_f32_e32 vcc, 0, v60
	v_mul_f32_e32 v59, v60, v60
	v_fmac_f32_e32 v59, 4.0, v58
	v_sqrt_f32_e32 v59, v59
	v_mul_f32_e32 v63, v62, v42
	v_mul_f32_e32 v43, v62, v40
	v_fma_f32 v40, v61, v40, -v63
	v_fma_f32 v42, v61, v42, v43
	v_add_f32_e64 v59, |v60|, v59
	v_add_f32_e32 v59, 0x0da24260, v59
	v_rcp_f32_e32 v59, v59
	v_add_f32_e32 v58, v57, v57
	v_mul_f32_e32 v59, v58, v59
	v_cndmask_b32_e64 v59, v59, -v59, vcc
	v_fma_f32 v58, v59, v59, 1.0
	v_rsq_f32_e32 v61, v58
	s_nop 0
	v_mul_f32_e32 v62, v61, v59
	v_mul_f32_e32 v55, v62, v54
	v_mul_f32_e32 v56, v62, v53
	v_fma_f32 v53, v61, v53, -v55
	v_fma_f32 v54, v61, v54, v56
	v_mul_f32_e32 v55, v52, v52
	v_mul_f32_e32 v56, v53, v53
	v_mul_f32_e32 v57, v52, v53
	v_add_f32_dpp v55, v55, v55 quad_perm:[1,0,3,2] row_mask:0xf bank_mask:0xf
	v_add_f32_dpp v56, v56, v56 quad_perm:[1,0,3,2] row_mask:0xf bank_mask:0xf
	v_add_f32_dpp v57, v57, v57 quad_perm:[1,0,3,2] row_mask:0xf bank_mask:0xf
	v_add_f32_dpp v55, v55, v55 quad_perm:[2,3,0,1] row_mask:0xf bank_mask:0xf
	v_add_f32_dpp v56, v56, v56 quad_perm:[2,3,0,1] row_mask:0xf bank_mask:0xf
	v_add_f32_dpp v57, v57, v57 quad_perm:[2,3,0,1] row_mask:0xf bank_mask:0xf
	v_sub_f32_e32 v60, v56, v55
	v_mul_f32_e32 v58, v57, v57
	v_cmp_gt_f32_e32 vcc, 0, v60
	v_mul_f32_e32 v59, v60, v60
	v_fmac_f32_e32 v59, 4.0, v58
	v_sqrt_f32_e32 v59, v59
	v_mul_f32_e32 v63, v62, v42
	v_mul_f32_e32 v43, v62, v41
	v_fma_f32 v41, v61, v41, -v63
	v_fma_f32 v42, v61, v42, v43
	v_add_f32_e64 v59, |v60|, v59
	v_add_f32_e32 v59, 0x0da24260, v59
	v_rcp_f32_e32 v59, v59
	v_add_f32_e32 v58, v57, v57
	v_mul_f32_e32 v59, v58, v59
	v_cndmask_b32_e64 v59, v59, -v59, vcc
	v_fma_f32 v58, v59, v59, 1.0
	v_rsq_f32_e32 v61, v58
	s_nop 0
	v_mul_f32_e32 v62, v61, v59
	v_mul_f32_e32 v55, v62, v53
	v_mul_f32_e32 v56, v62, v52
	v_fma_f32 v52, v61, v52, -v55
	v_fma_f32 v53, v61, v53, v56
	v_mul_f32_e32 v55, v52, v52
	v_mul_f32_e32 v56, v54, v54
	v_mul_f32_e32 v57, v52, v54
	v_add_f32_dpp v55, v55, v55 quad_perm:[1,0,3,2] row_mask:0xf bank_mask:0xf
	v_add_f32_dpp v56, v56, v56 quad_perm:[1,0,3,2] row_mask:0xf bank_mask:0xf
	v_add_f32_dpp v57, v57, v57 quad_perm:[1,0,3,2] row_mask:0xf bank_mask:0xf
	v_add_f32_dpp v55, v55, v55 quad_perm:[2,3,0,1] row_mask:0xf bank_mask:0xf
	v_add_f32_dpp v56, v56, v56 quad_perm:[2,3,0,1] row_mask:0xf bank_mask:0xf
	v_add_f32_dpp v57, v57, v57 quad_perm:[2,3,0,1] row_mask:0xf bank_mask:0xf
	v_sub_f32_e32 v60, v56, v55
	v_mul_f32_e32 v58, v57, v57
	v_cmp_gt_f32_e32 vcc, 0, v60
	v_mul_f32_e32 v59, v60, v60
	v_fmac_f32_e32 v59, 4.0, v58
	v_sqrt_f32_e32 v59, v59
	v_mul_f32_e32 v63, v62, v41
	v_mul_f32_e32 v43, v62, v40
	v_fma_f32 v40, v61, v40, -v63
	v_fma_f32 v41, v61, v41, v43
	v_add_f32_e64 v59, |v60|, v59
	v_add_f32_e32 v59, 0x0da24260, v59
	v_rcp_f32_e32 v59, v59
	v_add_f32_e32 v58, v57, v57
	v_mul_f32_e32 v59, v58, v59
	v_cndmask_b32_e64 v59, v59, -v59, vcc
	v_fma_f32 v58, v59, v59, 1.0
	v_rsq_f32_e32 v61, v58
	s_nop 0
	v_mul_f32_e32 v62, v61, v59
	v_mul_f32_e32 v55, v62, v54
	v_mul_f32_e32 v56, v62, v52
	v_fma_f32 v52, v61, v52, -v55
	v_fma_f32 v54, v61, v54, v56
	v_mul_f32_e32 v55, v53, v53
	v_mul_f32_e32 v56, v54, v54
	v_mul_f32_e32 v57, v53, v54
	v_add_f32_dpp v55, v55, v55 quad_perm:[1,0,3,2] row_mask:0xf bank_mask:0xf
	v_add_f32_dpp v56, v56, v56 quad_perm:[1,0,3,2] row_mask:0xf bank_mask:0xf
	v_add_f32_dpp v57, v57, v57 quad_perm:[1,0,3,2] row_mask:0xf bank_mask:0xf
	v_add_f32_dpp v55, v55, v55 quad_perm:[2,3,0,1] row_mask:0xf bank_mask:0xf
	v_add_f32_dpp v56, v56, v56 quad_perm:[2,3,0,1] row_mask:0xf bank_mask:0xf
	v_add_f32_dpp v57, v57, v57 quad_perm:[2,3,0,1] row_mask:0xf bank_mask:0xf
	v_sub_f32_e32 v60, v56, v55
	v_mul_f32_e32 v58, v57, v57
	v_cmp_gt_f32_e32 vcc, 0, v60
	v_mul_f32_e32 v59, v60, v60
	v_fmac_f32_e32 v59, 4.0, v58
	v_sqrt_f32_e32 v59, v59
	v_mul_f32_e32 v63, v62, v42
	v_mul_f32_e32 v43, v62, v40
	v_fma_f32 v40, v61, v40, -v63
	v_fma_f32 v42, v61, v42, v43
	v_add_f32_e64 v59, |v60|, v59
	v_add_f32_e32 v59, 0x0da24260, v59
	v_rcp_f32_e32 v59, v59
	v_add_f32_e32 v58, v57, v57
	v_mul_f32_e32 v59, v58, v59
	v_cndmask_b32_e64 v59, v59, -v59, vcc
	v_fma_f32 v58, v59, v59, 1.0
	v_rsq_f32_e32 v61, v58
	s_nop 0
	v_mul_f32_e32 v62, v61, v59
	v_mul_f32_e32 v55, v62, v54
	v_mul_f32_e32 v56, v62, v53
	v_fma_f32 v53, v61, v53, -v55
	v_fma_f32 v54, v61, v54, v56
	v_mul_f32_e32 v63, v62, v42
	v_mul_f32_e32 v43, v62, v41
	v_fma_f32 v41, v61, v41, -v63
	v_fma_f32 v42, v61, v42, v43
	v_mul_f32_e32 v55, v52, v52
	v_mul_f32_e32 v56, v53, v53
	v_mul_f32_e32 v57, v54, v54
	v_add_f32_dpp v55, v55, v55 quad_perm:[1,0,3,2] row_mask:0xf bank_mask:0xf
	v_add_f32_dpp v56, v56, v56 quad_perm:[1,0,3,2] row_mask:0xf bank_mask:0xf
	v_add_f32_dpp v57, v57, v57 quad_perm:[1,0,3,2] row_mask:0xf bank_mask:0xf
	v_add_f32_dpp v55, v55, v55 quad_perm:[2,3,0,1] row_mask:0xf bank_mask:0xf
	v_add_f32_dpp v56, v56, v56 quad_perm:[2,3,0,1] row_mask:0xf bank_mask:0xf
	v_add_f32_dpp v57, v57, v57 quad_perm:[2,3,0,1] row_mask:0xf bank_mask:0xf
	v_cmp_le_f32_e64 s[28:29], v55, v56
	v_cmp_le_f32_e64 s[30:31], v55, v57
	v_cmp_lt_f32_e32 vcc, v57, v56
	s_and_b64 s[28:29], s[28:29], s[30:31]
	s_andn2_b64 s[30:31], vcc, s[28:29]
	v_cndmask_b32_e64 v44, v52, v53, s[28:29]
	v_cndmask_b32_e64 v45, v54, v53, s[30:31]
	v_cndmask_b32_e64 v46, v40, v41, s[28:29]
	v_cndmask_b32_e64 v47, v42, v41, s[30:31]
	v_mul_f32_e32 v58, v44, v44
	s_nop 1
	v_add_f32_dpp v58, v58, v58 quad_perm:[1,0,3,2] row_mask:0xf bank_mask:0xf
	s_nop 1
	v_add_f32_dpp v58, v58, v58 quad_perm:[2,3,0,1] row_mask:0xf bank_mask:0xf
	v_max_f32_e32 v58, 0x3aa2425, v58
	v_rsq_f32_e32 v58, v58
	s_nop 0
	v_mul_f32_e32 v48, v44, v58
	v_mul_f32_e32 v59, v48, v45
	s_nop 1
	v_add_f32_dpp v59, v59, v59 quad_perm:[1,0,3,2] row_mask:0xf bank_mask:0xf
	s_nop 1
	v_add_f32_dpp v59, v59, v59 quad_perm:[2,3,0,1] row_mask:0xf bank_mask:0xf
	v_fma_f32 v49, -v59, v48, v45
	v_mul_f32_e32 v58, v49, v49
	s_nop 1
	v_add_f32_dpp v58, v58, v58 quad_perm:[1,0,3,2] row_mask:0xf bank_mask:0xf
	s_nop 1
	v_add_f32_dpp v58, v58, v58 quad_perm:[2,3,0,1] row_mask:0xf bank_mask:0xf
	v_max_f32_e32 v58, 0x3aa2425, v58
	v_rsq_f32_e32 v58, v58
	s_nop 0
	v_mul_f32_e32 v50, v49, v58
	v_mov_b32_dpp v43, v47 quad_perm:[2,0,1,3] row_mask:0xf bank_mask:0xf
	v_mov_b32_dpp v63, v47 quad_perm:[1,2,0,3] row_mask:0xf bank_mask:0xf
	v_mov_b32_dpp v62, v50 quad_perm:[2,0,1,3] row_mask:0xf bank_mask:0xf
	v_mov_b32_dpp v61, v50 quad_perm:[1,2,0,3] row_mask:0xf bank_mask:0xf
	v_mul_f32_dpp v60, v46, v43 quad_perm:[1,2,0,3] row_mask:0xf bank_mask:0xf
	v_mul_f32_dpp v51, v48, v62 quad_perm:[1,2,0,3] row_mask:0xf bank_mask:0xf
	s_nop 0
	v_fmac_f32_dpp v60, -v46, v63 quad_perm:[2,0,1,3] row_mask:0xf bank_mask:0xf
	v_fmac_f32_dpp v51, -v48, v61 quad_perm:[2,0,1,3] row_mask:0xf bank_mask:0xf
	v_mul_f32_dpp v52, v46, v48 quad_perm:[0,0,0,0] row_mask:0xf bank_mask:0xf
	v_mul_f32_dpp v53, v46, v48 quad_perm:[1,1,1,1] row_mask:0xf bank_mask:0xf
	v_mul_f32_dpp v54, v46, v48 quad_perm:[2,2,2,2] row_mask:0xf bank_mask:0xf
	v_fmac_f32_dpp v52, v47, v50 quad_perm:[0,0,0,0] row_mask:0xf bank_mask:0xf
	v_fmac_f32_dpp v53, v47, v50 quad_perm:[1,1,1,1] row_mask:0xf bank_mask:0xf
	v_fmac_f32_dpp v54, v47, v50 quad_perm:[2,2,2,2] row_mask:0xf bank_mask:0xf
	v_fmac_f32_dpp v52, v60, v51 quad_perm:[0,0,0,0] row_mask:0xf bank_mask:0xf
	v_fmac_f32_dpp v53, v60, v51 quad_perm:[1,1,1,1] row_mask:0xf bank_mask:0xf
	v_fmac_f32_dpp v54, v60, v51 quad_perm:[2,2,2,2] row_mask:0xf bank_mask:0xf
	v_mov_b32_e32 v55, 0
	v_writelane_b32 v55, s32, 48
	v_writelane_b32 v55, s33, 49
	v_writelane_b32 v55, s34, 50
	v_mul_f32_e32 v55, 0xbc800000, v55
	v_mul_f32_e32 v56, v55, v52
	v_mul_f32_e32 v57, v55, v53
	v_mul_f32_e32 v58, v55, v54
	v_add_f32_dpp v56, v56, v56 quad_perm:[1,0,3,2] row_mask:0xf bank_mask:0xf
	v_add_f32_dpp v57, v57, v57 quad_perm:[1,0,3,2] row_mask:0xf bank_mask:0xf
	v_add_f32_dpp v58, v58, v58 quad_perm:[1,0,3,2] row_mask:0xf bank_mask:0xf
	v_add_f32_dpp v56, v56, v56 quad_perm:[2,3,0,1] row_mask:0xf bank_mask:0xf
	v_add_f32_dpp v57, v57, v57 quad_perm:[2,3,0,1] row_mask:0xf bank_mask:0xf
	v_add_f32_dpp v58, v58, v58 quad_perm:[2,3,0,1] row_mask:0xf bank_mask:0xf
	v_cndmask_b32_e64 v52, v52, v56, s[26:27]
	v_cndmask_b32_e64 v53, v53, v57, s[26:27]
	v_cndmask_b32_e64 v54, v54, v58, s[26:27]
	v_subrev_u32_e32 v59, 48, v0
	v_lshlrev_b32_e32 v59, 4, v59
	s_mov_b32 s20, 0
	s_mov_b32 s21, 0xf0000
	s_mov_b64 exec, s[20:21]
	ds_write_b96 v59, v[52:54] offset:24576
	s_mov_b64 exec, -1
	s_waitcnt lgkmcnt(0)
	s_setprio 0
	s_branch .Ljoin
